# re-offset barrier of the trailing wave half moved from after the epilogue to the next unit's loop entry (its unit setup now overlaps the leading half's first load segment)
# speedup vs baseline: 1.0224x; 1.0224x over previous
.Lskipz_e1o:
	v_and_b32_e32 v130, 8, v187
	v_and_b32_e32 v131, 16, v187
	v_lshlrev_b32_e32 v130, 2, v130
	v_lshl_add_u32 v130, v131, 3, v130
	v_lshl_add_u32 v131, s4, 8, v185
	v_add_u32_e32 v130, v130, v131
	v_mov_b32_e32 v131, 0
	v_lshl_add_u64 v[130:131], v[130:131], 4, s[16:17]
	global_load_dwordx4 v[240:243], v[130:131], off
	global_load_dwordx2 v[244:245], v[130:131], off offset:256
	global_load_dword v184, v[130:131], off offset:264
	global_load_dword v189, v[130:131], off offset:268
	s_cmp_eq_u32 s53, 1
	s_cbranch_scc1 .Lnobar_e1o
	s_and_b64 vcc, exec, s[12:13]
	s_cbranch_vccz .Lnobar_e1o
	s_barrier
.Lnobar_e1o:
.LBB0_417:
	s_add_u32 s28, s6, 0xfffc0080
	s_addc_u32 s29, s7, -1
	s_add_i32 s43, 0, 0x10000
	s_cmp_eq_u32 s42, 12
	s_cselect_b32 s31, s5, s29
	s_cselect_b32 s30, s8, s28
	s_cselect_b32 s29, s9, s33
	s_cselect_b32 s28, s21, s23
	s_add_i32 s63, 0, 0x14000
	v_add_u32_e32 v142, s43, v186
	v_add_u32_e32 v168, s63, v186
	ds_read_b128 v[130:133], v142
	ds_read_b128 v[134:137], v142 offset:1024
	ds_read_b128 v[138:141], v142 offset:2048
	ds_read_b128 v[142:145], v142 offset:3072
	ds_read_b128 v[146:149], v168
	ds_read_b128 v[150:153], v168 offset:1024
	ds_read_b128 v[154:157], v168 offset:2048
	ds_read_b128 v[168:171], v168 offset:3072
	v_lshl_add_u64 v[216:217], s[6:7], 0, v[166:167]
	s_add_i32 m0, s45, 0xc000
	ds_read_b128 v[172:175], v188
	ds_read_b128 v[176:179], v188 offset:1024
	ds_read_b128 v[180:183], v188 offset:2048
	ds_read_b128 v[190:193], v188 offset:3072
	ds_read_b128 v[194:197], v188 offset:4096
	ds_read_b128 v[198:201], v188 offset:5120
	ds_read_b128 v[202:205], v188 offset:6144
	ds_read_b128 v[206:209], v188 offset:7168
	global_load_lds_dwordx4 v[216:217], off
	v_lshl_add_u64 v[216:217], s[6:7], 0, v[164:165]
	s_add_i32 m0, s45, 0xe000
	s_nop 0
	global_load_lds_dwordx4 v[216:217], off
	s_waitcnt vmcnt(8)
	s_waitcnt lgkmcnt(0)
	s_barrier
	s_setprio 1
	s_waitcnt lgkmcnt(0)
	v_mfma_f32_16x16x32_bf16 v[126:129], v[130:133], v[172:175], v[126:129]
	v_mfma_f32_16x16x32_bf16 v[122:125], v[138:141], v[172:175], v[122:125]
	v_mfma_f32_16x16x32_bf16 v[114:117], v[130:133], v[180:183], v[114:117]
	v_mfma_f32_16x16x32_bf16 v[106:109], v[138:141], v[180:183], v[106:109]
	v_mfma_f32_16x16x32_bf16 v[98:101], v[130:133], v[194:197], v[98:101]
	v_mfma_f32_16x16x32_bf16 v[90:93], v[138:141], v[194:197], v[90:93]
	v_mfma_f32_16x16x32_bf16 v[82:85], v[130:133], v[202:205], v[82:85]
	v_mfma_f32_16x16x32_bf16 v[74:77], v[138:141], v[202:205], v[74:77]
	v_mfma_f32_16x16x32_bf16 v[126:129], v[134:137], v[176:179], v[126:129]
	v_mfma_f32_16x16x32_bf16 v[122:125], v[142:145], v[176:179], v[122:125]
	v_mfma_f32_16x16x32_bf16 v[114:117], v[134:137], v[190:193], v[114:117]
	v_mfma_f32_16x16x32_bf16 v[106:109], v[142:145], v[190:193], v[106:109]
	v_mfma_f32_16x16x32_bf16 v[98:101], v[134:137], v[198:201], v[98:101]
	v_mfma_f32_16x16x32_bf16 v[90:93], v[142:145], v[198:201], v[90:93]
	v_mfma_f32_16x16x32_bf16 v[82:85], v[134:137], v[206:209], v[82:85]
	v_mfma_f32_16x16x32_bf16 v[74:77], v[142:145], v[206:209], v[74:77]
	s_setprio 0
	s_setprio 1
	v_mfma_f32_16x16x32_bf16 v[118:121], v[146:149], v[172:175], v[118:121]
	v_mfma_f32_16x16x32_bf16 v[110:113], v[154:157], v[172:175], v[110:113]
	v_mfma_f32_16x16x32_bf16 v[102:105], v[146:149], v[180:183], v[102:105]
	v_mfma_f32_16x16x32_bf16 v[94:97], v[154:157], v[180:183], v[94:97]
	v_mfma_f32_16x16x32_bf16 v[86:89], v[146:149], v[194:197], v[86:89]
	v_mfma_f32_16x16x32_bf16 v[78:81], v[154:157], v[194:197], v[78:81]
	v_mfma_f32_16x16x32_bf16 v[70:73], v[146:149], v[202:205], v[70:73]
	v_mfma_f32_16x16x32_bf16 v[66:69], v[154:157], v[202:205], v[66:69]
	v_mfma_f32_16x16x32_bf16 v[118:121], v[150:153], v[176:179], v[118:121]
	v_mfma_f32_16x16x32_bf16 v[110:113], v[168:171], v[176:179], v[110:113]
	v_mfma_f32_16x16x32_bf16 v[102:105], v[150:153], v[190:193], v[102:105]
	v_mfma_f32_16x16x32_bf16 v[94:97], v[168:171], v[190:193], v[94:97]
	v_mfma_f32_16x16x32_bf16 v[86:89], v[150:153], v[198:201], v[86:89]
	v_mfma_f32_16x16x32_bf16 v[78:81], v[168:171], v[198:201], v[78:81]
	v_mfma_f32_16x16x32_bf16 v[70:73], v[150:153], v[206:209], v[70:73]
	v_mfma_f32_16x16x32_bf16 v[66:69], v[168:171], v[206:209], v[66:69]
	s_setprio 0
	s_barrier
	s_add_i32 s43, s43, s44
	v_lshl_add_u64 v[216:217], s[28:29], 0, v[0:1]
	s_mov_b32 m0, s43
	ds_read_b128 v[172:175], v188 offset:16384
	ds_read_b128 v[176:179], v188 offset:17408
	ds_read_b128 v[180:183], v188 offset:18432
	ds_read_b128 v[190:193], v188 offset:19456
	ds_read_b128 v[194:197], v188 offset:20480
	ds_read_b128 v[198:201], v188 offset:21504
	ds_read_b128 v[202:205], v188 offset:22528
	ds_read_b128 v[206:209], v188 offset:23552
	global_load_lds_dwordx4 v[216:217], off
	s_add_i32 m0, s43, 0x2000
	s_add_u32 s58, s28, 0x40000
	v_lshl_add_u64 v[218:219], s[28:29], 0, v[158:159]
	s_addc_u32 s59, s29, 0
	s_add_i32 s43, s63, s44
	global_load_lds_dwordx4 v[218:219], off
	v_lshl_add_u64 v[220:221], s[58:59], 0, v[0:1]
	s_mov_b32 m0, s43
	v_lshl_add_u64 v[222:223], s[30:31], 0, v[160:161]
	global_load_lds_dwordx4 v[220:221], off
	v_lshl_add_u64 v[220:221], s[58:59], 0, v[158:159]
	s_add_i32 m0, s43, 0x2000
	s_nop 0
	global_load_lds_dwordx4 v[220:221], off
	v_lshl_add_u64 v[220:221], s[30:31], 0, v[162:163]
	s_mov_b32 m0, s45
	s_nop 0
	global_load_lds_dwordx4 v[220:221], off
	s_mov_b32 m0, s46
	s_nop 0
	global_load_lds_dwordx4 v[222:223], off
	s_waitcnt vmcnt(8)
	s_waitcnt lgkmcnt(0)
	s_barrier
	s_setprio 1
	s_waitcnt lgkmcnt(0)
	v_mfma_f32_16x16x32_bf16 v[62:65], v[130:133], v[172:175], v[62:65]
	v_mfma_f32_16x16x32_bf16 v[58:61], v[138:141], v[172:175], v[58:61]
	v_mfma_f32_16x16x32_bf16 v[50:53], v[130:133], v[180:183], v[50:53]
	v_mfma_f32_16x16x32_bf16 v[42:45], v[138:141], v[180:183], v[42:45]
	v_mfma_f32_16x16x32_bf16 v[34:37], v[130:133], v[194:197], v[34:37]
	v_mfma_f32_16x16x32_bf16 v[26:29], v[138:141], v[194:197], v[26:29]
	v_mfma_f32_16x16x32_bf16 v[18:21], v[130:133], v[202:205], v[18:21]
	v_mfma_f32_16x16x32_bf16 v[10:13], v[138:141], v[202:205], v[10:13]
	v_mfma_f32_16x16x32_bf16 v[62:65], v[134:137], v[176:179], v[62:65]
	v_mfma_f32_16x16x32_bf16 v[58:61], v[142:145], v[176:179], v[58:61]
	v_mfma_f32_16x16x32_bf16 v[50:53], v[134:137], v[190:193], v[50:53]
	v_mfma_f32_16x16x32_bf16 v[42:45], v[142:145], v[190:193], v[42:45]
	v_mfma_f32_16x16x32_bf16 v[34:37], v[134:137], v[198:201], v[34:37]
	v_mfma_f32_16x16x32_bf16 v[26:29], v[142:145], v[198:201], v[26:29]
	v_mfma_f32_16x16x32_bf16 v[18:21], v[134:137], v[206:209], v[18:21]
	v_mfma_f32_16x16x32_bf16 v[10:13], v[142:145], v[206:209], v[10:13]
	s_setprio 0
	s_setprio 1
	v_mfma_f32_16x16x32_bf16 v[54:57], v[146:149], v[172:175], v[54:57]
	v_mfma_f32_16x16x32_bf16 v[46:49], v[154:157], v[172:175], v[46:49]
	v_mfma_f32_16x16x32_bf16 v[38:41], v[146:149], v[180:183], v[38:41]
	v_mfma_f32_16x16x32_bf16 v[30:33], v[154:157], v[180:183], v[30:33]
	v_mfma_f32_16x16x32_bf16 v[22:25], v[146:149], v[194:197], v[22:25]
	v_mfma_f32_16x16x32_bf16 v[14:17], v[154:157], v[194:197], v[14:17]
	v_mfma_f32_16x16x32_bf16 v[6:9], v[146:149], v[202:205], v[6:9]
	v_mfma_f32_16x16x32_bf16 v[2:5], v[154:157], v[202:205], v[2:5]
	v_mfma_f32_16x16x32_bf16 v[54:57], v[150:153], v[176:179], v[54:57]
	v_mfma_f32_16x16x32_bf16 v[46:49], v[168:171], v[176:179], v[46:49]
	v_mfma_f32_16x16x32_bf16 v[38:41], v[150:153], v[190:193], v[38:41]
	v_mfma_f32_16x16x32_bf16 v[30:33], v[168:171], v[190:193], v[30:33]
	v_mfma_f32_16x16x32_bf16 v[22:25], v[150:153], v[198:201], v[22:25]
	v_mfma_f32_16x16x32_bf16 v[14:17], v[168:171], v[198:201], v[14:17]
	v_mfma_f32_16x16x32_bf16 v[6:9], v[150:153], v[206:209], v[6:9]
	v_mfma_f32_16x16x32_bf16 v[2:5], v[168:171], v[206:209], v[2:5]
	s_setprio 0
	s_barrier
	s_add_i32 s43, 0, 0x18000
	s_add_i32 s58, 0, 0x1c000
	v_add_u32_e32 v142, s43, v186
	v_add_u32_e32 v168, s58, v186
	ds_read_b128 v[130:133], v142
	ds_read_b128 v[134:137], v142 offset:1024
	ds_read_b128 v[138:141], v142 offset:2048
	ds_read_b128 v[142:145], v142 offset:3072
	ds_read_b128 v[146:149], v168
	ds_read_b128 v[150:153], v168 offset:1024
	ds_read_b128 v[154:157], v168 offset:2048
	ds_read_b128 v[168:171], v168 offset:3072
	s_add_u32 s30, s30, 0x40000
	s_addc_u32 s31, s31, 0
	s_mov_b32 m0, s47
	v_lshl_add_u64 v[224:225], s[30:31], 0, v[162:163]
	ds_read_b128 v[172:175], v188 offset:32768
	ds_read_b128 v[176:179], v188 offset:33792
	ds_read_b128 v[180:183], v188 offset:34816
	ds_read_b128 v[190:193], v188 offset:35840
	ds_read_b128 v[194:197], v188 offset:36864
	ds_read_b128 v[198:201], v188 offset:37888
	ds_read_b128 v[202:205], v188 offset:38912
	ds_read_b128 v[206:209], v188 offset:39936
	global_load_lds_dwordx4 v[224:225], off
	v_lshl_add_u64 v[224:225], s[30:31], 0, v[160:161]
	s_mov_b32 m0, s48
	s_nop 0
	global_load_lds_dwordx4 v[224:225], off
	s_waitcnt vmcnt(8)
	s_waitcnt lgkmcnt(0)
	s_barrier
	s_setprio 1
	s_waitcnt lgkmcnt(0)
	v_mfma_f32_16x16x32_bf16 v[126:129], v[130:133], v[172:175], v[126:129]
	v_mfma_f32_16x16x32_bf16 v[122:125], v[138:141], v[172:175], v[122:125]
	v_mfma_f32_16x16x32_bf16 v[114:117], v[130:133], v[180:183], v[114:117]
	v_mfma_f32_16x16x32_bf16 v[106:109], v[138:141], v[180:183], v[106:109]
	v_mfma_f32_16x16x32_bf16 v[98:101], v[130:133], v[194:197], v[98:101]
	v_mfma_f32_16x16x32_bf16 v[90:93], v[138:141], v[194:197], v[90:93]
	v_mfma_f32_16x16x32_bf16 v[82:85], v[130:133], v[202:205], v[82:85]
	v_mfma_f32_16x16x32_bf16 v[74:77], v[138:141], v[202:205], v[74:77]
	v_mfma_f32_16x16x32_bf16 v[126:129], v[134:137], v[176:179], v[126:129]
	v_mfma_f32_16x16x32_bf16 v[122:125], v[142:145], v[176:179], v[122:125]
	v_mfma_f32_16x16x32_bf16 v[114:117], v[134:137], v[190:193], v[114:117]
	v_mfma_f32_16x16x32_bf16 v[106:109], v[142:145], v[190:193], v[106:109]
	v_mfma_f32_16x16x32_bf16 v[98:101], v[134:137], v[198:201], v[98:101]
	v_mfma_f32_16x16x32_bf16 v[90:93], v[142:145], v[198:201], v[90:93]
	v_mfma_f32_16x16x32_bf16 v[82:85], v[134:137], v[206:209], v[82:85]
	v_mfma_f32_16x16x32_bf16 v[74:77], v[142:145], v[206:209], v[74:77]
	s_setprio 0
	s_setprio 1
	v_mfma_f32_16x16x32_bf16 v[118:121], v[146:149], v[172:175], v[118:121]
	v_mfma_f32_16x16x32_bf16 v[110:113], v[154:157], v[172:175], v[110:113]
	v_mfma_f32_16x16x32_bf16 v[102:105], v[146:149], v[180:183], v[102:105]
	v_mfma_f32_16x16x32_bf16 v[94:97], v[154:157], v[180:183], v[94:97]
	v_mfma_f32_16x16x32_bf16 v[86:89], v[146:149], v[194:197], v[86:89]
	v_mfma_f32_16x16x32_bf16 v[78:81], v[154:157], v[194:197], v[78:81]
	v_mfma_f32_16x16x32_bf16 v[70:73], v[146:149], v[202:205], v[70:73]
	v_mfma_f32_16x16x32_bf16 v[66:69], v[154:157], v[202:205], v[66:69]
	v_mfma_f32_16x16x32_bf16 v[118:121], v[150:153], v[176:179], v[118:121]
	v_mfma_f32_16x16x32_bf16 v[110:113], v[168:171], v[176:179], v[110:113]
	v_mfma_f32_16x16x32_bf16 v[102:105], v[150:153], v[190:193], v[102:105]
	v_mfma_f32_16x16x32_bf16 v[94:97], v[168:171], v[190:193], v[94:97]
	v_mfma_f32_16x16x32_bf16 v[86:89], v[150:153], v[198:201], v[86:89]
	v_mfma_f32_16x16x32_bf16 v[78:81], v[168:171], v[198:201], v[78:81]
	v_mfma_f32_16x16x32_bf16 v[70:73], v[150:153], v[206:209], v[70:73]
	v_mfma_f32_16x16x32_bf16 v[66:69], v[168:171], v[206:209], v[66:69]
	s_setprio 0
	s_barrier
	s_add_i32 s30, s43, s44
	v_lshl_add_u64 v[216:217], v[216:217], 0, s[56:57]
	s_mov_b32 m0, s30
	ds_read_b128 v[172:175], v188 offset:49152
	ds_read_b128 v[176:179], v188 offset:50176
	ds_read_b128 v[180:183], v188 offset:51200
	ds_read_b128 v[190:193], v188 offset:52224
	ds_read_b128 v[194:197], v188 offset:53248
	ds_read_b128 v[198:201], v188 offset:54272
	ds_read_b128 v[202:205], v188 offset:55296
	ds_read_b128 v[206:209], v188 offset:56320
	global_load_lds_dwordx4 v[216:217], off
	s_add_i32 m0, s30, 0x2000
	s_add_u32 s28, s28, 0x40080
	v_lshl_add_u64 v[216:217], v[218:219], 0, s[56:57]
	s_addc_u32 s29, s29, 0
	s_add_i32 s30, s58, s44
	global_load_lds_dwordx4 v[216:217], off
	v_lshl_add_u64 v[216:217], s[28:29], 0, v[0:1]
	s_mov_b32 m0, s30
	s_nop 0
	global_load_lds_dwordx4 v[216:217], off
	v_lshl_add_u64 v[216:217], s[28:29], 0, v[158:159]
	s_add_i32 m0, s30, 0x2000
	s_nop 0
	global_load_lds_dwordx4 v[216:217], off
	v_lshl_add_u64 v[216:217], v[220:221], 0, s[56:57]
	s_mov_b32 m0, s49
	s_nop 0
	global_load_lds_dwordx4 v[216:217], off
	v_lshl_add_u64 v[216:217], v[222:223], 0, s[56:57]
	s_mov_b32 m0, s52
	s_nop 0
	global_load_lds_dwordx4 v[216:217], off
	s_waitcnt vmcnt(8)
	s_waitcnt lgkmcnt(0)
	s_barrier
	s_setprio 1
	s_waitcnt lgkmcnt(0)
	v_mfma_f32_16x16x32_bf16 v[62:65], v[130:133], v[172:175], v[62:65]
	v_mfma_f32_16x16x32_bf16 v[58:61], v[138:141], v[172:175], v[58:61]
	v_mfma_f32_16x16x32_bf16 v[50:53], v[130:133], v[180:183], v[50:53]
	v_mfma_f32_16x16x32_bf16 v[42:45], v[138:141], v[180:183], v[42:45]
	v_mfma_f32_16x16x32_bf16 v[34:37], v[130:133], v[194:197], v[34:37]
	v_mfma_f32_16x16x32_bf16 v[26:29], v[138:141], v[194:197], v[26:29]
	v_mfma_f32_16x16x32_bf16 v[18:21], v[130:133], v[202:205], v[18:21]
	v_mfma_f32_16x16x32_bf16 v[10:13], v[138:141], v[202:205], v[10:13]
	v_mfma_f32_16x16x32_bf16 v[62:65], v[134:137], v[176:179], v[62:65]
	v_mfma_f32_16x16x32_bf16 v[58:61], v[142:145], v[176:179], v[58:61]
	v_mfma_f32_16x16x32_bf16 v[50:53], v[134:137], v[190:193], v[50:53]
	v_mfma_f32_16x16x32_bf16 v[42:45], v[142:145], v[190:193], v[42:45]
	v_mfma_f32_16x16x32_bf16 v[34:37], v[134:137], v[198:201], v[34:37]
	v_mfma_f32_16x16x32_bf16 v[26:29], v[142:145], v[198:201], v[26:29]
	v_mfma_f32_16x16x32_bf16 v[18:21], v[134:137], v[206:209], v[18:21]
	v_mfma_f32_16x16x32_bf16 v[10:13], v[142:145], v[206:209], v[10:13]
	s_setprio 0
	s_setprio 1
	v_mfma_f32_16x16x32_bf16 v[54:57], v[146:149], v[172:175], v[54:57]
	v_mfma_f32_16x16x32_bf16 v[46:49], v[154:157], v[172:175], v[46:49]
	v_mfma_f32_16x16x32_bf16 v[38:41], v[146:149], v[180:183], v[38:41]
	v_mfma_f32_16x16x32_bf16 v[30:33], v[154:157], v[180:183], v[30:33]
	v_mfma_f32_16x16x32_bf16 v[22:25], v[146:149], v[194:197], v[22:25]
	v_mfma_f32_16x16x32_bf16 v[14:17], v[154:157], v[194:197], v[14:17]
	v_mfma_f32_16x16x32_bf16 v[6:9], v[146:149], v[202:205], v[6:9]
	v_mfma_f32_16x16x32_bf16 v[2:5], v[154:157], v[202:205], v[2:5]
	v_mfma_f32_16x16x32_bf16 v[54:57], v[150:153], v[176:179], v[54:57]
	v_mfma_f32_16x16x32_bf16 v[46:49], v[168:171], v[176:179], v[46:49]
	v_mfma_f32_16x16x32_bf16 v[38:41], v[150:153], v[190:193], v[38:41]
	v_mfma_f32_16x16x32_bf16 v[30:33], v[168:171], v[190:193], v[30:33]
	v_mfma_f32_16x16x32_bf16 v[22:25], v[150:153], v[198:201], v[22:25]
	v_mfma_f32_16x16x32_bf16 v[14:17], v[168:171], v[198:201], v[14:17]
	v_mfma_f32_16x16x32_bf16 v[6:9], v[150:153], v[206:209], v[6:9]
	v_mfma_f32_16x16x32_bf16 v[2:5], v[168:171], v[206:209], v[2:5]
	s_setprio 0
	s_barrier
	s_add_i32 s42, s42, 2
	s_add_u32 s23, s23, 0x100
	s_addc_u32 s33, s33, 0
	s_add_u32 s6, s6, 0x100
	s_addc_u32 s7, s7, 0
	s_cmp_gt_u32 s42, 13
	s_cbranch_scc0 .LBB0_417
	s_and_b64 vcc, exec, s[18:19]
	s_cbranch_vccz .LBB0_420
	s_barrier
.LBB0_420:
	v_mov_b32_e32 v200, 0
	v_mov_b32_e32 v201, 0
	v_mov_b32_e32 v202, 0
	v_mov_b32_e32 v203, 0
	v_lshl_add_u32 v182, s4, 8, v185
	s_cmp_gt_u32 s62, 3
	s_cselect_b64 s[4:5], -1, 0
	v_cndmask_b32_e64 v190, v230, 1.0, s[4:5]
	s_waitcnt vmcnt(8)
	v_add_f32_e32 v240, v240, v241
	v_add_f32_e32 v242, v242, v243
	v_add_f32_e32 v240, v240, v242
	v_fmamk_f32 v240, v240, 0x3a800000, v226
	v_rsq_f32_e32 v240, v240
	v_add_f32_e32 v244, v244, v245
	v_add_f32_e32 v184, v184, v189
	v_add_f32_e32 v244, v244, v184
	v_fmamk_f32 v244, v244, 0x3a800000, v226
	v_rsq_f32_e32 v244, v244
	v_and_b32_e32 v191, 15, v185
	v_lshlrev_b32_e32 v191, 2, v191
	v_add_u32_e32 v192, 64, v191
	v_add_u32_e32 v193, 0x80, v191
	v_add_u32_e32 v194, 0xc0, v191
	v_mul_f32_e32 v240, v240, v190
	v_mul_f32_e32 v244, v244, v190
	ds_bpermute_b32 v144, v191, v240
	ds_bpermute_b32 v146, v191, v244
	ds_bpermute_b32 v148, v192, v240
	ds_bpermute_b32 v150, v192, v244
	ds_bpermute_b32 v152, v193, v240
	ds_bpermute_b32 v154, v193, v244
	ds_bpermute_b32 v156, v194, v240
	ds_bpermute_b32 v168, v194, v244
	v_lshl_or_b32 v170, s62, 8, v187
	v_lshlrev_b32_e32 v170, 1, v170
	v_mov_b32_e32 v171, 0
	v_mov_b64_e32 v[172:173], s[14:15]
	v_mad_i64_i32 v[172:173], s[4:5], v182, s69, v[172:173]
	v_lshl_add_u64 v[172:173], v[172:173], 0, v[170:171]
	s_waitcnt lgkmcnt(0)
	v_pk_mul_f32 v[126:127], v[126:127], v[144:145] op_sel_hi:[1,0]
	v_pk_mul_f32 v[128:129], v[128:129], v[144:145] op_sel_hi:[1,0]
	v_pk_mul_f32 v[122:123], v[122:123], v[144:145] op_sel_hi:[1,0]
	v_pk_mul_f32 v[124:125], v[124:125], v[144:145] op_sel_hi:[1,0]
	v_cvt_pk_bf16_f32 v126, v126, v127
	v_cvt_pk_bf16_f32 v127, v128, v129
	v_cvt_pk_bf16_f32 v128, v122, v123
	v_cvt_pk_bf16_f32 v129, v124, v125
	global_store_dwordx4 v[172:173], v[126:129], off
	v_pk_mul_f32 v[118:119], v[118:119], v[144:145] op_sel_hi:[1,0]
	v_pk_mul_f32 v[120:121], v[120:121], v[144:145] op_sel_hi:[1,0]
	v_pk_mul_f32 v[110:111], v[110:111], v[144:145] op_sel_hi:[1,0]
	v_pk_mul_f32 v[112:113], v[112:113], v[144:145] op_sel_hi:[1,0]
	v_cvt_pk_bf16_f32 v118, v118, v119
	v_cvt_pk_bf16_f32 v119, v120, v121
	v_cvt_pk_bf16_f32 v120, v110, v111
	v_cvt_pk_bf16_f32 v121, v112, v113
	global_store_dwordx4 v[172:173], v[118:121], off offset:256
	s_mov_b64 s[42:43], 0xa000
	v_lshl_add_u64 v[176:177], v[172:173], 0, s[42:43]
	v_pk_mul_f32 v[114:115], v[114:115], v[146:147] op_sel_hi:[1,0]
	v_pk_mul_f32 v[116:117], v[116:117], v[146:147] op_sel_hi:[1,0]
	v_pk_mul_f32 v[106:107], v[106:107], v[146:147] op_sel_hi:[1,0]
	v_pk_mul_f32 v[108:109], v[108:109], v[146:147] op_sel_hi:[1,0]
	v_cvt_pk_bf16_f32 v114, v114, v115
	v_cvt_pk_bf16_f32 v115, v116, v117
	v_cvt_pk_bf16_f32 v116, v106, v107
	v_cvt_pk_bf16_f32 v117, v108, v109
	global_store_dwordx4 v[176:177], v[114:117], off
	v_pk_mul_f32 v[102:103], v[102:103], v[146:147] op_sel_hi:[1,0]
	v_pk_mul_f32 v[104:105], v[104:105], v[146:147] op_sel_hi:[1,0]
	v_pk_mul_f32 v[94:95], v[94:95], v[146:147] op_sel_hi:[1,0]
	v_pk_mul_f32 v[96:97], v[96:97], v[146:147] op_sel_hi:[1,0]
	v_cvt_pk_bf16_f32 v102, v102, v103
	v_cvt_pk_bf16_f32 v103, v104, v105
	v_cvt_pk_bf16_f32 v104, v94, v95
	v_cvt_pk_bf16_f32 v105, v96, v97
	global_store_dwordx4 v[176:177], v[102:105], off offset:256
	s_mov_b64 s[42:43], 0x14000
	v_lshl_add_u64 v[174:175], v[172:173], 0, s[42:43]
	v_pk_mul_f32 v[98:99], v[98:99], v[148:149] op_sel_hi:[1,0]
	v_pk_mul_f32 v[100:101], v[100:101], v[148:149] op_sel_hi:[1,0]
	v_pk_mul_f32 v[90:91], v[90:91], v[148:149] op_sel_hi:[1,0]
	v_pk_mul_f32 v[92:93], v[92:93], v[148:149] op_sel_hi:[1,0]
	v_cvt_pk_bf16_f32 v98, v98, v99
	v_cvt_pk_bf16_f32 v99, v100, v101
	v_cvt_pk_bf16_f32 v100, v90, v91
	v_cvt_pk_bf16_f32 v101, v92, v93
	global_store_dwordx4 v[174:175], v[98:101], off
	v_pk_mul_f32 v[86:87], v[86:87], v[148:149] op_sel_hi:[1,0]
	v_pk_mul_f32 v[88:89], v[88:89], v[148:149] op_sel_hi:[1,0]
	v_pk_mul_f32 v[78:79], v[78:79], v[148:149] op_sel_hi:[1,0]
	v_pk_mul_f32 v[80:81], v[80:81], v[148:149] op_sel_hi:[1,0]
	v_cvt_pk_bf16_f32 v86, v86, v87
	v_cvt_pk_bf16_f32 v87, v88, v89
	v_cvt_pk_bf16_f32 v88, v78, v79
	v_cvt_pk_bf16_f32 v89, v80, v81
	global_store_dwordx4 v[174:175], v[86:89], off offset:256
	s_mov_b64 s[42:43], 0x1e000
	v_lshl_add_u64 v[176:177], v[172:173], 0, s[42:43]
	v_pk_mul_f32 v[82:83], v[82:83], v[150:151] op_sel_hi:[1,0]
	v_pk_mul_f32 v[84:85], v[84:85], v[150:151] op_sel_hi:[1,0]
	v_pk_mul_f32 v[74:75], v[74:75], v[150:151] op_sel_hi:[1,0]
	v_pk_mul_f32 v[76:77], v[76:77], v[150:151] op_sel_hi:[1,0]
	v_cvt_pk_bf16_f32 v82, v82, v83
	v_cvt_pk_bf16_f32 v83, v84, v85
	v_cvt_pk_bf16_f32 v84, v74, v75
	v_cvt_pk_bf16_f32 v85, v76, v77
	global_store_dwordx4 v[176:177], v[82:85], off
	v_pk_mul_f32 v[70:71], v[70:71], v[150:151] op_sel_hi:[1,0]
	v_pk_mul_f32 v[72:73], v[72:73], v[150:151] op_sel_hi:[1,0]
	v_pk_mul_f32 v[66:67], v[66:67], v[150:151] op_sel_hi:[1,0]
	v_pk_mul_f32 v[68:69], v[68:69], v[150:151] op_sel_hi:[1,0]
	v_cvt_pk_bf16_f32 v70, v70, v71
	v_cvt_pk_bf16_f32 v71, v72, v73
	v_cvt_pk_bf16_f32 v72, v66, v67
	v_cvt_pk_bf16_f32 v73, v68, v69
	global_store_dwordx4 v[176:177], v[70:73], off offset:256
	s_mov_b64 s[42:43], 0x50000
	v_lshl_add_u64 v[174:175], v[172:173], 0, s[42:43]
	v_pk_mul_f32 v[62:63], v[62:63], v[152:153] op_sel_hi:[1,0]
	v_pk_mul_f32 v[64:65], v[64:65], v[152:153] op_sel_hi:[1,0]
	v_pk_mul_f32 v[58:59], v[58:59], v[152:153] op_sel_hi:[1,0]
	v_pk_mul_f32 v[60:61], v[60:61], v[152:153] op_sel_hi:[1,0]
	v_cvt_pk_bf16_f32 v62, v62, v63
	v_cvt_pk_bf16_f32 v63, v64, v65
	v_cvt_pk_bf16_f32 v64, v58, v59
	v_cvt_pk_bf16_f32 v65, v60, v61
	global_store_dwordx4 v[174:175], v[62:65], off
	v_pk_mul_f32 v[54:55], v[54:55], v[152:153] op_sel_hi:[1,0]
	v_pk_mul_f32 v[56:57], v[56:57], v[152:153] op_sel_hi:[1,0]
	v_pk_mul_f32 v[46:47], v[46:47], v[152:153] op_sel_hi:[1,0]
	v_pk_mul_f32 v[48:49], v[48:49], v[152:153] op_sel_hi:[1,0]
	v_cvt_pk_bf16_f32 v54, v54, v55
	v_cvt_pk_bf16_f32 v55, v56, v57
	v_cvt_pk_bf16_f32 v56, v46, v47
	v_cvt_pk_bf16_f32 v57, v48, v49
	global_store_dwordx4 v[174:175], v[54:57], off offset:256
	s_mov_b64 s[42:43], 0x5a000
	v_lshl_add_u64 v[176:177], v[172:173], 0, s[42:43]
	v_pk_mul_f32 v[50:51], v[50:51], v[154:155] op_sel_hi:[1,0]
	v_pk_mul_f32 v[52:53], v[52:53], v[154:155] op_sel_hi:[1,0]
	v_pk_mul_f32 v[42:43], v[42:43], v[154:155] op_sel_hi:[1,0]
	v_pk_mul_f32 v[44:45], v[44:45], v[154:155] op_sel_hi:[1,0]
	v_cvt_pk_bf16_f32 v50, v50, v51
	v_cvt_pk_bf16_f32 v51, v52, v53
	v_cvt_pk_bf16_f32 v52, v42, v43
	v_cvt_pk_bf16_f32 v53, v44, v45
	global_store_dwordx4 v[176:177], v[50:53], off
	v_pk_mul_f32 v[38:39], v[38:39], v[154:155] op_sel_hi:[1,0]
	v_pk_mul_f32 v[40:41], v[40:41], v[154:155] op_sel_hi:[1,0]
	v_pk_mul_f32 v[30:31], v[30:31], v[154:155] op_sel_hi:[1,0]
	v_pk_mul_f32 v[32:33], v[32:33], v[154:155] op_sel_hi:[1,0]
	v_cvt_pk_bf16_f32 v38, v38, v39
	v_cvt_pk_bf16_f32 v39, v40, v41
	v_cvt_pk_bf16_f32 v40, v30, v31
	v_cvt_pk_bf16_f32 v41, v32, v33
	global_store_dwordx4 v[176:177], v[38:41], off offset:256
	s_mov_b64 s[42:43], 0x64000
	v_lshl_add_u64 v[174:175], v[172:173], 0, s[42:43]
	v_pk_mul_f32 v[34:35], v[34:35], v[156:157] op_sel_hi:[1,0]
	v_pk_mul_f32 v[36:37], v[36:37], v[156:157] op_sel_hi:[1,0]
	v_pk_mul_f32 v[26:27], v[26:27], v[156:157] op_sel_hi:[1,0]
	v_pk_mul_f32 v[28:29], v[28:29], v[156:157] op_sel_hi:[1,0]
	v_cvt_pk_bf16_f32 v34, v34, v35
	v_cvt_pk_bf16_f32 v35, v36, v37
	v_cvt_pk_bf16_f32 v36, v26, v27
	v_cvt_pk_bf16_f32 v37, v28, v29
	global_store_dwordx4 v[174:175], v[34:37], off
	v_pk_mul_f32 v[22:23], v[22:23], v[156:157] op_sel_hi:[1,0]
	v_pk_mul_f32 v[24:25], v[24:25], v[156:157] op_sel_hi:[1,0]
	v_pk_mul_f32 v[14:15], v[14:15], v[156:157] op_sel_hi:[1,0]
	v_pk_mul_f32 v[16:17], v[16:17], v[156:157] op_sel_hi:[1,0]
	v_cvt_pk_bf16_f32 v22, v22, v23
	v_cvt_pk_bf16_f32 v23, v24, v25
	v_cvt_pk_bf16_f32 v24, v14, v15
	v_cvt_pk_bf16_f32 v25, v16, v17
	global_store_dwordx4 v[174:175], v[22:25], off offset:256
	s_mov_b64 s[42:43], 0x6e000
	v_lshl_add_u64 v[176:177], v[172:173], 0, s[42:43]
	v_pk_mul_f32 v[18:19], v[18:19], v[168:169] op_sel_hi:[1,0]
	v_pk_mul_f32 v[20:21], v[20:21], v[168:169] op_sel_hi:[1,0]
	v_pk_mul_f32 v[10:11], v[10:11], v[168:169] op_sel_hi:[1,0]
	v_pk_mul_f32 v[12:13], v[12:13], v[168:169] op_sel_hi:[1,0]
	v_cvt_pk_bf16_f32 v18, v18, v19
	v_cvt_pk_bf16_f32 v19, v20, v21
	v_cvt_pk_bf16_f32 v20, v10, v11
	v_cvt_pk_bf16_f32 v21, v12, v13
	global_store_dwordx4 v[176:177], v[18:21], off
	v_pk_mul_f32 v[6:7], v[6:7], v[168:169] op_sel_hi:[1,0]
	v_pk_mul_f32 v[8:9], v[8:9], v[168:169] op_sel_hi:[1,0]
	v_pk_mul_f32 v[2:3], v[2:3], v[168:169] op_sel_hi:[1,0]
	v_pk_mul_f32 v[4:5], v[4:5], v[168:169] op_sel_hi:[1,0]
	v_cvt_pk_bf16_f32 v6, v6, v7
	v_cvt_pk_bf16_f32 v7, v8, v9
	v_cvt_pk_bf16_f32 v8, v2, v3
	v_cvt_pk_bf16_f32 v9, v4, v5
	global_store_dwordx4 v[176:177], v[6:9], off offset:256
	s_nop 3
	v_mfma_f32_32x32x16_bf16 v[2:17], v[200:203], v[200:203], 0
	v_mfma_f32_32x32x16_bf16 v[18:33], v[200:203], v[200:203], 0
	v_mfma_f32_32x32x16_bf16 v[34:49], v[200:203], v[200:203], 0
	v_mfma_f32_32x32x16_bf16 v[50:65], v[200:203], v[200:203], 0
	v_mfma_f32_32x32x16_bf16 v[66:81], v[200:203], v[200:203], 0
	v_mfma_f32_32x32x16_bf16 v[82:97], v[200:203], v[200:203], 0
	v_mfma_f32_32x32x16_bf16 v[98:113], v[200:203], v[200:203], 0
	v_mfma_f32_32x32x16_bf16 v[114:129], v[200:203], v[200:203], 0
	s_andn2_b64 vcc, exec, s[40:41]
	s_mov_b64 s[6:7], -1
	s_cbranch_vccnz .LBB0_413
	s_andn2_b64 vcc, exec, s[12:13]
	s_cbranch_vccnz .LBB0_412
	s_branch .LBB0_412

.Lskipz_e1e:
	v_and_b32_e32 v130, 8, v187
	v_and_b32_e32 v131, 16, v187
	v_lshlrev_b32_e32 v130, 2, v130
	v_lshl_add_u32 v130, v131, 3, v130
	v_lshl_add_u32 v131, s4, 8, v185
	v_add_u32_e32 v130, v130, v131
	v_mov_b32_e32 v131, 0
	v_lshl_add_u64 v[130:131], v[130:131], 4, s[16:17]
	global_load_dwordx4 v[240:243], v[130:131], off
	global_load_dwordx2 v[244:245], v[130:131], off offset:256
	global_load_dword v184, v[130:131], off offset:264
	global_load_dword v189, v[130:131], off offset:268
	s_cmp_eq_u32 s49, 1
	s_cbranch_scc1 .Lnobar_e1e
	s_and_b64 vcc, exec, s[12:13]
	s_cbranch_vccz .Lnobar_e1e
	s_barrier
.Lnobar_e1e:
.LBB0_836:
	s_add_u32 s28, s6, 0xfffc0080
	s_addc_u32 s29, s7, -1
	s_add_i32 s41, 0, 0x10000
	s_cmp_eq_u32 s40, 12
	s_cselect_b32 s31, s5, s29
	s_cselect_b32 s30, s8, s28
	s_cselect_b32 s29, s9, s33
	s_cselect_b32 s28, s21, s23
	s_add_i32 s53, 0, 0x14000
	v_add_u32_e32 v142, s41, v186
	v_add_u32_e32 v168, s53, v186
	ds_read_b128 v[130:133], v142
	ds_read_b128 v[134:137], v142 offset:1024
	ds_read_b128 v[138:141], v142 offset:2048
	ds_read_b128 v[142:145], v142 offset:3072
	ds_read_b128 v[146:149], v168
	ds_read_b128 v[150:153], v168 offset:1024
	ds_read_b128 v[154:157], v168 offset:2048
	ds_read_b128 v[168:171], v168 offset:3072
	v_lshl_add_u64 v[216:217], s[6:7], 0, v[166:167]
	s_add_i32 m0, s43, 0xc000
	ds_read_b128 v[172:175], v188
	ds_read_b128 v[176:179], v188 offset:1024
	ds_read_b128 v[180:183], v188 offset:2048
	ds_read_b128 v[190:193], v188 offset:3072
	ds_read_b128 v[194:197], v188 offset:4096
	ds_read_b128 v[198:201], v188 offset:5120
	ds_read_b128 v[202:205], v188 offset:6144
	ds_read_b128 v[206:209], v188 offset:7168
	global_load_lds_dwordx4 v[216:217], off
	v_lshl_add_u64 v[216:217], s[6:7], 0, v[164:165]
	s_add_i32 m0, s43, 0xe000
	s_nop 0
	global_load_lds_dwordx4 v[216:217], off
	s_waitcnt vmcnt(8)
	s_waitcnt lgkmcnt(0)
	s_barrier
	s_setprio 1
	s_waitcnt lgkmcnt(0)
	v_mfma_f32_16x16x32_bf16 v[126:129], v[130:133], v[172:175], v[126:129]
	v_mfma_f32_16x16x32_bf16 v[122:125], v[138:141], v[172:175], v[122:125]
	v_mfma_f32_16x16x32_bf16 v[114:117], v[130:133], v[180:183], v[114:117]
	v_mfma_f32_16x16x32_bf16 v[106:109], v[138:141], v[180:183], v[106:109]
	v_mfma_f32_16x16x32_bf16 v[98:101], v[130:133], v[194:197], v[98:101]
	v_mfma_f32_16x16x32_bf16 v[90:93], v[138:141], v[194:197], v[90:93]
	v_mfma_f32_16x16x32_bf16 v[82:85], v[130:133], v[202:205], v[82:85]
	v_mfma_f32_16x16x32_bf16 v[74:77], v[138:141], v[202:205], v[74:77]
	v_mfma_f32_16x16x32_bf16 v[126:129], v[134:137], v[176:179], v[126:129]
	v_mfma_f32_16x16x32_bf16 v[122:125], v[142:145], v[176:179], v[122:125]
	v_mfma_f32_16x16x32_bf16 v[114:117], v[134:137], v[190:193], v[114:117]
	v_mfma_f32_16x16x32_bf16 v[106:109], v[142:145], v[190:193], v[106:109]
	v_mfma_f32_16x16x32_bf16 v[98:101], v[134:137], v[198:201], v[98:101]
	v_mfma_f32_16x16x32_bf16 v[90:93], v[142:145], v[198:201], v[90:93]
	v_mfma_f32_16x16x32_bf16 v[82:85], v[134:137], v[206:209], v[82:85]
	v_mfma_f32_16x16x32_bf16 v[74:77], v[142:145], v[206:209], v[74:77]
	s_setprio 0
	s_setprio 1
	v_mfma_f32_16x16x32_bf16 v[118:121], v[146:149], v[172:175], v[118:121]
	v_mfma_f32_16x16x32_bf16 v[110:113], v[154:157], v[172:175], v[110:113]
	v_mfma_f32_16x16x32_bf16 v[102:105], v[146:149], v[180:183], v[102:105]
	v_mfma_f32_16x16x32_bf16 v[94:97], v[154:157], v[180:183], v[94:97]
	v_mfma_f32_16x16x32_bf16 v[86:89], v[146:149], v[194:197], v[86:89]
	v_mfma_f32_16x16x32_bf16 v[78:81], v[154:157], v[194:197], v[78:81]
	v_mfma_f32_16x16x32_bf16 v[70:73], v[146:149], v[202:205], v[70:73]
	v_mfma_f32_16x16x32_bf16 v[66:69], v[154:157], v[202:205], v[66:69]
	v_mfma_f32_16x16x32_bf16 v[118:121], v[150:153], v[176:179], v[118:121]
	v_mfma_f32_16x16x32_bf16 v[110:113], v[168:171], v[176:179], v[110:113]
	v_mfma_f32_16x16x32_bf16 v[102:105], v[150:153], v[190:193], v[102:105]
	v_mfma_f32_16x16x32_bf16 v[94:97], v[168:171], v[190:193], v[94:97]
	v_mfma_f32_16x16x32_bf16 v[86:89], v[150:153], v[198:201], v[86:89]
	v_mfma_f32_16x16x32_bf16 v[78:81], v[168:171], v[198:201], v[78:81]
	v_mfma_f32_16x16x32_bf16 v[70:73], v[150:153], v[206:209], v[70:73]
	v_mfma_f32_16x16x32_bf16 v[66:69], v[168:171], v[206:209], v[66:69]
	s_setprio 0
	s_barrier
	s_add_i32 s41, s41, s42
	v_lshl_add_u64 v[216:217], s[28:29], 0, v[0:1]
	s_mov_b32 m0, s41
	ds_read_b128 v[172:175], v188 offset:16384
	ds_read_b128 v[176:179], v188 offset:17408
	ds_read_b128 v[180:183], v188 offset:18432
	ds_read_b128 v[190:193], v188 offset:19456
	ds_read_b128 v[194:197], v188 offset:20480
	ds_read_b128 v[198:201], v188 offset:21504
	ds_read_b128 v[202:205], v188 offset:22528
	ds_read_b128 v[206:209], v188 offset:23552
	global_load_lds_dwordx4 v[216:217], off
	s_add_i32 m0, s41, 0x2000
	s_add_u32 s58, s28, 0x40000
	v_lshl_add_u64 v[218:219], s[28:29], 0, v[158:159]
	s_addc_u32 s59, s29, 0
	s_add_i32 s41, s53, s42
	global_load_lds_dwordx4 v[218:219], off
	v_lshl_add_u64 v[220:221], s[58:59], 0, v[0:1]
	s_mov_b32 m0, s41
	v_lshl_add_u64 v[222:223], s[30:31], 0, v[160:161]
	global_load_lds_dwordx4 v[220:221], off
	v_lshl_add_u64 v[220:221], s[58:59], 0, v[158:159]
	s_add_i32 m0, s41, 0x2000
	s_nop 0
	global_load_lds_dwordx4 v[220:221], off
	v_lshl_add_u64 v[220:221], s[30:31], 0, v[162:163]
	s_mov_b32 m0, s43
	s_nop 0
	global_load_lds_dwordx4 v[220:221], off
	s_mov_b32 m0, s44
	s_nop 0
	global_load_lds_dwordx4 v[222:223], off
	s_waitcnt vmcnt(8)
	s_waitcnt lgkmcnt(0)
	s_barrier
	s_setprio 1
	s_waitcnt lgkmcnt(0)
	v_mfma_f32_16x16x32_bf16 v[62:65], v[130:133], v[172:175], v[62:65]
	v_mfma_f32_16x16x32_bf16 v[58:61], v[138:141], v[172:175], v[58:61]
	v_mfma_f32_16x16x32_bf16 v[50:53], v[130:133], v[180:183], v[50:53]
	v_mfma_f32_16x16x32_bf16 v[42:45], v[138:141], v[180:183], v[42:45]
	v_mfma_f32_16x16x32_bf16 v[34:37], v[130:133], v[194:197], v[34:37]
	v_mfma_f32_16x16x32_bf16 v[26:29], v[138:141], v[194:197], v[26:29]
	v_mfma_f32_16x16x32_bf16 v[18:21], v[130:133], v[202:205], v[18:21]
	v_mfma_f32_16x16x32_bf16 v[10:13], v[138:141], v[202:205], v[10:13]
	v_mfma_f32_16x16x32_bf16 v[62:65], v[134:137], v[176:179], v[62:65]
	v_mfma_f32_16x16x32_bf16 v[58:61], v[142:145], v[176:179], v[58:61]
	v_mfma_f32_16x16x32_bf16 v[50:53], v[134:137], v[190:193], v[50:53]
	v_mfma_f32_16x16x32_bf16 v[42:45], v[142:145], v[190:193], v[42:45]
	v_mfma_f32_16x16x32_bf16 v[34:37], v[134:137], v[198:201], v[34:37]
	v_mfma_f32_16x16x32_bf16 v[26:29], v[142:145], v[198:201], v[26:29]
	v_mfma_f32_16x16x32_bf16 v[18:21], v[134:137], v[206:209], v[18:21]
	v_mfma_f32_16x16x32_bf16 v[10:13], v[142:145], v[206:209], v[10:13]
	s_setprio 0
	s_setprio 1
	v_mfma_f32_16x16x32_bf16 v[54:57], v[146:149], v[172:175], v[54:57]
	v_mfma_f32_16x16x32_bf16 v[46:49], v[154:157], v[172:175], v[46:49]
	v_mfma_f32_16x16x32_bf16 v[38:41], v[146:149], v[180:183], v[38:41]
	v_mfma_f32_16x16x32_bf16 v[30:33], v[154:157], v[180:183], v[30:33]
	v_mfma_f32_16x16x32_bf16 v[22:25], v[146:149], v[194:197], v[22:25]
	v_mfma_f32_16x16x32_bf16 v[14:17], v[154:157], v[194:197], v[14:17]
	v_mfma_f32_16x16x32_bf16 v[6:9], v[146:149], v[202:205], v[6:9]
	v_mfma_f32_16x16x32_bf16 v[2:5], v[154:157], v[202:205], v[2:5]
	v_mfma_f32_16x16x32_bf16 v[54:57], v[150:153], v[176:179], v[54:57]
	v_mfma_f32_16x16x32_bf16 v[46:49], v[168:171], v[176:179], v[46:49]
	v_mfma_f32_16x16x32_bf16 v[38:41], v[150:153], v[190:193], v[38:41]
	v_mfma_f32_16x16x32_bf16 v[30:33], v[168:171], v[190:193], v[30:33]
	v_mfma_f32_16x16x32_bf16 v[22:25], v[150:153], v[198:201], v[22:25]
	v_mfma_f32_16x16x32_bf16 v[14:17], v[168:171], v[198:201], v[14:17]
	v_mfma_f32_16x16x32_bf16 v[6:9], v[150:153], v[206:209], v[6:9]
	v_mfma_f32_16x16x32_bf16 v[2:5], v[168:171], v[206:209], v[2:5]
	s_setprio 0
	s_barrier
	s_add_i32 s41, 0, 0x18000
	s_add_i32 s53, 0, 0x1c000
	v_add_u32_e32 v142, s41, v186
	v_add_u32_e32 v168, s53, v186
	ds_read_b128 v[130:133], v142
	ds_read_b128 v[134:137], v142 offset:1024
	ds_read_b128 v[138:141], v142 offset:2048
	ds_read_b128 v[142:145], v142 offset:3072
	ds_read_b128 v[146:149], v168
	ds_read_b128 v[150:153], v168 offset:1024
	ds_read_b128 v[154:157], v168 offset:2048
	ds_read_b128 v[168:171], v168 offset:3072
	s_add_u32 s30, s30, 0x40000
	s_addc_u32 s31, s31, 0
	s_mov_b32 m0, s45
	v_lshl_add_u64 v[224:225], s[30:31], 0, v[162:163]
	ds_read_b128 v[172:175], v188 offset:32768
	ds_read_b128 v[176:179], v188 offset:33792
	ds_read_b128 v[180:183], v188 offset:34816
	ds_read_b128 v[190:193], v188 offset:35840
	ds_read_b128 v[194:197], v188 offset:36864
	ds_read_b128 v[198:201], v188 offset:37888
	ds_read_b128 v[202:205], v188 offset:38912
	ds_read_b128 v[206:209], v188 offset:39936
	global_load_lds_dwordx4 v[224:225], off
	v_lshl_add_u64 v[224:225], s[30:31], 0, v[160:161]
	s_mov_b32 m0, s46
	s_nop 0
	global_load_lds_dwordx4 v[224:225], off
	s_waitcnt vmcnt(8)
	s_waitcnt lgkmcnt(0)
	s_barrier
	s_setprio 1
	s_waitcnt lgkmcnt(0)
	v_mfma_f32_16x16x32_bf16 v[126:129], v[130:133], v[172:175], v[126:129]
	v_mfma_f32_16x16x32_bf16 v[122:125], v[138:141], v[172:175], v[122:125]
	v_mfma_f32_16x16x32_bf16 v[114:117], v[130:133], v[180:183], v[114:117]
	v_mfma_f32_16x16x32_bf16 v[106:109], v[138:141], v[180:183], v[106:109]
	v_mfma_f32_16x16x32_bf16 v[98:101], v[130:133], v[194:197], v[98:101]
	v_mfma_f32_16x16x32_bf16 v[90:93], v[138:141], v[194:197], v[90:93]
	v_mfma_f32_16x16x32_bf16 v[82:85], v[130:133], v[202:205], v[82:85]
	v_mfma_f32_16x16x32_bf16 v[74:77], v[138:141], v[202:205], v[74:77]
	v_mfma_f32_16x16x32_bf16 v[126:129], v[134:137], v[176:179], v[126:129]
	v_mfma_f32_16x16x32_bf16 v[122:125], v[142:145], v[176:179], v[122:125]
	v_mfma_f32_16x16x32_bf16 v[114:117], v[134:137], v[190:193], v[114:117]
	v_mfma_f32_16x16x32_bf16 v[106:109], v[142:145], v[190:193], v[106:109]
	v_mfma_f32_16x16x32_bf16 v[98:101], v[134:137], v[198:201], v[98:101]
	v_mfma_f32_16x16x32_bf16 v[90:93], v[142:145], v[198:201], v[90:93]
	v_mfma_f32_16x16x32_bf16 v[82:85], v[134:137], v[206:209], v[82:85]
	v_mfma_f32_16x16x32_bf16 v[74:77], v[142:145], v[206:209], v[74:77]
	s_setprio 0
	s_setprio 1
	v_mfma_f32_16x16x32_bf16 v[118:121], v[146:149], v[172:175], v[118:121]
	v_mfma_f32_16x16x32_bf16 v[110:113], v[154:157], v[172:175], v[110:113]
	v_mfma_f32_16x16x32_bf16 v[102:105], v[146:149], v[180:183], v[102:105]
	v_mfma_f32_16x16x32_bf16 v[94:97], v[154:157], v[180:183], v[94:97]
	v_mfma_f32_16x16x32_bf16 v[86:89], v[146:149], v[194:197], v[86:89]
	v_mfma_f32_16x16x32_bf16 v[78:81], v[154:157], v[194:197], v[78:81]
	v_mfma_f32_16x16x32_bf16 v[70:73], v[146:149], v[202:205], v[70:73]
	v_mfma_f32_16x16x32_bf16 v[66:69], v[154:157], v[202:205], v[66:69]
	v_mfma_f32_16x16x32_bf16 v[118:121], v[150:153], v[176:179], v[118:121]
	v_mfma_f32_16x16x32_bf16 v[110:113], v[168:171], v[176:179], v[110:113]
	v_mfma_f32_16x16x32_bf16 v[102:105], v[150:153], v[190:193], v[102:105]
	v_mfma_f32_16x16x32_bf16 v[94:97], v[168:171], v[190:193], v[94:97]
	v_mfma_f32_16x16x32_bf16 v[86:89], v[150:153], v[198:201], v[86:89]
	v_mfma_f32_16x16x32_bf16 v[78:81], v[168:171], v[198:201], v[78:81]
	v_mfma_f32_16x16x32_bf16 v[70:73], v[150:153], v[206:209], v[70:73]
	v_mfma_f32_16x16x32_bf16 v[66:69], v[168:171], v[206:209], v[66:69]
	s_setprio 0
	s_barrier
	s_add_i32 s30, s41, s42
	v_lshl_add_u64 v[216:217], v[216:217], 0, s[56:57]
	s_mov_b32 m0, s30
	ds_read_b128 v[172:175], v188 offset:49152
	ds_read_b128 v[176:179], v188 offset:50176
	ds_read_b128 v[180:183], v188 offset:51200
	ds_read_b128 v[190:193], v188 offset:52224
	ds_read_b128 v[194:197], v188 offset:53248
	ds_read_b128 v[198:201], v188 offset:54272
	ds_read_b128 v[202:205], v188 offset:55296
	ds_read_b128 v[206:209], v188 offset:56320
	global_load_lds_dwordx4 v[216:217], off
	s_add_i32 m0, s30, 0x2000
	s_add_u32 s28, s28, 0x40080
	v_lshl_add_u64 v[216:217], v[218:219], 0, s[56:57]
	s_addc_u32 s29, s29, 0
	s_add_i32 s30, s53, s42
	global_load_lds_dwordx4 v[216:217], off
	v_lshl_add_u64 v[216:217], s[28:29], 0, v[0:1]
	s_mov_b32 m0, s30
	s_nop 0
	global_load_lds_dwordx4 v[216:217], off
	v_lshl_add_u64 v[216:217], s[28:29], 0, v[158:159]
	s_add_i32 m0, s30, 0x2000
	s_nop 0
	global_load_lds_dwordx4 v[216:217], off
	v_lshl_add_u64 v[216:217], v[220:221], 0, s[56:57]
	s_mov_b32 m0, s47
	s_nop 0
	global_load_lds_dwordx4 v[216:217], off
	v_lshl_add_u64 v[216:217], v[222:223], 0, s[56:57]
	s_mov_b32 m0, s48
	s_nop 0
	global_load_lds_dwordx4 v[216:217], off
	s_waitcnt vmcnt(8)
	s_waitcnt lgkmcnt(0)
	s_barrier
	s_setprio 1
	s_waitcnt lgkmcnt(0)
	v_mfma_f32_16x16x32_bf16 v[62:65], v[130:133], v[172:175], v[62:65]
	v_mfma_f32_16x16x32_bf16 v[58:61], v[138:141], v[172:175], v[58:61]
	v_mfma_f32_16x16x32_bf16 v[50:53], v[130:133], v[180:183], v[50:53]
	v_mfma_f32_16x16x32_bf16 v[42:45], v[138:141], v[180:183], v[42:45]
	v_mfma_f32_16x16x32_bf16 v[34:37], v[130:133], v[194:197], v[34:37]
	v_mfma_f32_16x16x32_bf16 v[26:29], v[138:141], v[194:197], v[26:29]
	v_mfma_f32_16x16x32_bf16 v[18:21], v[130:133], v[202:205], v[18:21]
	v_mfma_f32_16x16x32_bf16 v[10:13], v[138:141], v[202:205], v[10:13]
	v_mfma_f32_16x16x32_bf16 v[62:65], v[134:137], v[176:179], v[62:65]
	v_mfma_f32_16x16x32_bf16 v[58:61], v[142:145], v[176:179], v[58:61]
	v_mfma_f32_16x16x32_bf16 v[50:53], v[134:137], v[190:193], v[50:53]
	v_mfma_f32_16x16x32_bf16 v[42:45], v[142:145], v[190:193], v[42:45]
	v_mfma_f32_16x16x32_bf16 v[34:37], v[134:137], v[198:201], v[34:37]
	v_mfma_f32_16x16x32_bf16 v[26:29], v[142:145], v[198:201], v[26:29]
	v_mfma_f32_16x16x32_bf16 v[18:21], v[134:137], v[206:209], v[18:21]
	v_mfma_f32_16x16x32_bf16 v[10:13], v[142:145], v[206:209], v[10:13]
	s_setprio 0
	s_setprio 1
	v_mfma_f32_16x16x32_bf16 v[54:57], v[146:149], v[172:175], v[54:57]
	v_mfma_f32_16x16x32_bf16 v[46:49], v[154:157], v[172:175], v[46:49]
	v_mfma_f32_16x16x32_bf16 v[38:41], v[146:149], v[180:183], v[38:41]
	v_mfma_f32_16x16x32_bf16 v[30:33], v[154:157], v[180:183], v[30:33]
	v_mfma_f32_16x16x32_bf16 v[22:25], v[146:149], v[194:197], v[22:25]
	v_mfma_f32_16x16x32_bf16 v[14:17], v[154:157], v[194:197], v[14:17]
	v_mfma_f32_16x16x32_bf16 v[6:9], v[146:149], v[202:205], v[6:9]
	v_mfma_f32_16x16x32_bf16 v[2:5], v[154:157], v[202:205], v[2:5]
	v_mfma_f32_16x16x32_bf16 v[54:57], v[150:153], v[176:179], v[54:57]
	v_mfma_f32_16x16x32_bf16 v[46:49], v[168:171], v[176:179], v[46:49]
	v_mfma_f32_16x16x32_bf16 v[38:41], v[150:153], v[190:193], v[38:41]
	v_mfma_f32_16x16x32_bf16 v[30:33], v[168:171], v[190:193], v[30:33]
	v_mfma_f32_16x16x32_bf16 v[22:25], v[150:153], v[198:201], v[22:25]
	v_mfma_f32_16x16x32_bf16 v[14:17], v[168:171], v[198:201], v[14:17]
	v_mfma_f32_16x16x32_bf16 v[6:9], v[150:153], v[206:209], v[6:9]
	v_mfma_f32_16x16x32_bf16 v[2:5], v[168:171], v[206:209], v[2:5]
	s_setprio 0
	s_barrier
	s_add_i32 s40, s40, 2
	s_add_u32 s23, s23, 0x100
	s_addc_u32 s33, s33, 0
	s_add_u32 s6, s6, 0x100
	s_addc_u32 s7, s7, 0
	s_cmp_gt_u32 s40, 13
	s_cbranch_scc0 .LBB0_836
	s_and_b64 vcc, exec, s[18:19]
	s_cbranch_vccz .LBB0_839
	s_barrier
.LBB0_839:
	v_mov_b32_e32 v200, 0
	v_mov_b32_e32 v201, 0
	v_mov_b32_e32 v202, 0
	v_mov_b32_e32 v203, 0
	v_lshl_add_u32 v182, s4, 8, v185
	s_lshl_b32 s4, 1, s52
	s_and_b32 s4, s4, 0x18f
	s_cmp_eq_u32 s4, 0
	s_cselect_b64 s[4:5], -1, 0
	v_cndmask_b32_e64 v190, v230, 1.0, s[4:5]
	s_waitcnt vmcnt(8)
	v_add_f32_e32 v240, v240, v241
	v_add_f32_e32 v242, v242, v243
	v_add_f32_e32 v240, v240, v242
	v_fmamk_f32 v240, v240, 0x3a800000, v226
	v_rsq_f32_e32 v240, v240
	v_add_f32_e32 v244, v244, v245
	v_add_f32_e32 v184, v184, v189
	v_add_f32_e32 v244, v244, v184
	v_fmamk_f32 v244, v244, 0x3a800000, v226
	v_rsq_f32_e32 v244, v244
	v_and_b32_e32 v191, 15, v185
	v_lshlrev_b32_e32 v191, 2, v191
	v_add_u32_e32 v192, 64, v191
	v_add_u32_e32 v193, 0x80, v191
	v_add_u32_e32 v194, 0xc0, v191
	v_mul_f32_e32 v240, v240, v190
	v_mul_f32_e32 v244, v244, v190
	ds_bpermute_b32 v144, v191, v240
	ds_bpermute_b32 v146, v191, v244
	ds_bpermute_b32 v148, v192, v240
	ds_bpermute_b32 v150, v192, v244
	ds_bpermute_b32 v152, v193, v240
	ds_bpermute_b32 v154, v193, v244
	ds_bpermute_b32 v156, v194, v240
	ds_bpermute_b32 v168, v194, v244
	s_movk_i32 s6, 0x1a00
	v_lshl_or_b32 v170, s52, 8, v187
	v_lshlrev_b32_e32 v170, 1, v170
	v_mov_b32_e32 v171, 0
	v_mov_b64_e32 v[172:173], s[14:15]
	v_mad_i64_i32 v[172:173], s[4:5], v182, s6, v[172:173]
	v_lshl_add_u64 v[172:173], v[172:173], 0, v[170:171]
	s_waitcnt lgkmcnt(0)
	v_pk_mul_f32 v[126:127], v[126:127], v[144:145] op_sel_hi:[1,0]
	v_pk_mul_f32 v[128:129], v[128:129], v[144:145] op_sel_hi:[1,0]
	v_pk_mul_f32 v[122:123], v[122:123], v[144:145] op_sel_hi:[1,0]
	v_pk_mul_f32 v[124:125], v[124:125], v[144:145] op_sel_hi:[1,0]
	v_cvt_pk_bf16_f32 v126, v126, v127
	v_cvt_pk_bf16_f32 v127, v128, v129
	v_cvt_pk_bf16_f32 v128, v122, v123
	v_cvt_pk_bf16_f32 v129, v124, v125
	global_store_dwordx4 v[172:173], v[126:129], off
	v_pk_mul_f32 v[118:119], v[118:119], v[144:145] op_sel_hi:[1,0]
	v_pk_mul_f32 v[120:121], v[120:121], v[144:145] op_sel_hi:[1,0]
	v_pk_mul_f32 v[110:111], v[110:111], v[144:145] op_sel_hi:[1,0]
	v_pk_mul_f32 v[112:113], v[112:113], v[144:145] op_sel_hi:[1,0]
	v_cvt_pk_bf16_f32 v118, v118, v119
	v_cvt_pk_bf16_f32 v119, v120, v121
	v_cvt_pk_bf16_f32 v120, v110, v111
	v_cvt_pk_bf16_f32 v121, v112, v113
	global_store_dwordx4 v[172:173], v[118:121], off offset:256
	s_mov_b64 s[40:41], 0x1a000
	v_lshl_add_u64 v[176:177], v[172:173], 0, s[40:41]
	v_pk_mul_f32 v[114:115], v[114:115], v[146:147] op_sel_hi:[1,0]
	v_pk_mul_f32 v[116:117], v[116:117], v[146:147] op_sel_hi:[1,0]
	v_pk_mul_f32 v[106:107], v[106:107], v[146:147] op_sel_hi:[1,0]
	v_pk_mul_f32 v[108:109], v[108:109], v[146:147] op_sel_hi:[1,0]
	v_cvt_pk_bf16_f32 v114, v114, v115
	v_cvt_pk_bf16_f32 v115, v116, v117
	v_cvt_pk_bf16_f32 v116, v106, v107
	v_cvt_pk_bf16_f32 v117, v108, v109
	global_store_dwordx4 v[176:177], v[114:117], off
	v_pk_mul_f32 v[102:103], v[102:103], v[146:147] op_sel_hi:[1,0]
	v_pk_mul_f32 v[104:105], v[104:105], v[146:147] op_sel_hi:[1,0]
	v_pk_mul_f32 v[94:95], v[94:95], v[146:147] op_sel_hi:[1,0]
	v_pk_mul_f32 v[96:97], v[96:97], v[146:147] op_sel_hi:[1,0]
	v_cvt_pk_bf16_f32 v102, v102, v103
	v_cvt_pk_bf16_f32 v103, v104, v105
	v_cvt_pk_bf16_f32 v104, v94, v95
	v_cvt_pk_bf16_f32 v105, v96, v97
	global_store_dwordx4 v[176:177], v[102:105], off offset:256
	s_mov_b64 s[40:41], 0x34000
	v_lshl_add_u64 v[174:175], v[172:173], 0, s[40:41]
	v_pk_mul_f32 v[98:99], v[98:99], v[148:149] op_sel_hi:[1,0]
	v_pk_mul_f32 v[100:101], v[100:101], v[148:149] op_sel_hi:[1,0]
	v_pk_mul_f32 v[90:91], v[90:91], v[148:149] op_sel_hi:[1,0]
	v_pk_mul_f32 v[92:93], v[92:93], v[148:149] op_sel_hi:[1,0]
	v_cvt_pk_bf16_f32 v98, v98, v99
	v_cvt_pk_bf16_f32 v99, v100, v101
	v_cvt_pk_bf16_f32 v100, v90, v91
	v_cvt_pk_bf16_f32 v101, v92, v93
	global_store_dwordx4 v[174:175], v[98:101], off
	v_pk_mul_f32 v[86:87], v[86:87], v[148:149] op_sel_hi:[1,0]
	v_pk_mul_f32 v[88:89], v[88:89], v[148:149] op_sel_hi:[1,0]
	v_pk_mul_f32 v[78:79], v[78:79], v[148:149] op_sel_hi:[1,0]
	v_pk_mul_f32 v[80:81], v[80:81], v[148:149] op_sel_hi:[1,0]
	v_cvt_pk_bf16_f32 v86, v86, v87
	v_cvt_pk_bf16_f32 v87, v88, v89
	v_cvt_pk_bf16_f32 v88, v78, v79
	v_cvt_pk_bf16_f32 v89, v80, v81
	global_store_dwordx4 v[174:175], v[86:89], off offset:256
	s_mov_b64 s[40:41], 0x4e000
	v_lshl_add_u64 v[176:177], v[172:173], 0, s[40:41]
	v_pk_mul_f32 v[82:83], v[82:83], v[150:151] op_sel_hi:[1,0]
	v_pk_mul_f32 v[84:85], v[84:85], v[150:151] op_sel_hi:[1,0]
	v_pk_mul_f32 v[74:75], v[74:75], v[150:151] op_sel_hi:[1,0]
	v_pk_mul_f32 v[76:77], v[76:77], v[150:151] op_sel_hi:[1,0]
	v_cvt_pk_bf16_f32 v82, v82, v83
	v_cvt_pk_bf16_f32 v83, v84, v85
	v_cvt_pk_bf16_f32 v84, v74, v75
	v_cvt_pk_bf16_f32 v85, v76, v77
	global_store_dwordx4 v[176:177], v[82:85], off
	v_pk_mul_f32 v[70:71], v[70:71], v[150:151] op_sel_hi:[1,0]
	v_pk_mul_f32 v[72:73], v[72:73], v[150:151] op_sel_hi:[1,0]
	v_pk_mul_f32 v[66:67], v[66:67], v[150:151] op_sel_hi:[1,0]
	v_pk_mul_f32 v[68:69], v[68:69], v[150:151] op_sel_hi:[1,0]
	v_cvt_pk_bf16_f32 v70, v70, v71
	v_cvt_pk_bf16_f32 v71, v72, v73
	v_cvt_pk_bf16_f32 v72, v66, v67
	v_cvt_pk_bf16_f32 v73, v68, v69
	global_store_dwordx4 v[176:177], v[70:73], off offset:256
	s_mov_b64 s[40:41], 0xd0000
	v_lshl_add_u64 v[174:175], v[172:173], 0, s[40:41]
	v_pk_mul_f32 v[62:63], v[62:63], v[152:153] op_sel_hi:[1,0]
	v_pk_mul_f32 v[64:65], v[64:65], v[152:153] op_sel_hi:[1,0]
	v_pk_mul_f32 v[58:59], v[58:59], v[152:153] op_sel_hi:[1,0]
	v_pk_mul_f32 v[60:61], v[60:61], v[152:153] op_sel_hi:[1,0]
	v_cvt_pk_bf16_f32 v62, v62, v63
	v_cvt_pk_bf16_f32 v63, v64, v65
	v_cvt_pk_bf16_f32 v64, v58, v59
	v_cvt_pk_bf16_f32 v65, v60, v61
	global_store_dwordx4 v[174:175], v[62:65], off
	v_pk_mul_f32 v[54:55], v[54:55], v[152:153] op_sel_hi:[1,0]
	v_pk_mul_f32 v[56:57], v[56:57], v[152:153] op_sel_hi:[1,0]
	v_pk_mul_f32 v[46:47], v[46:47], v[152:153] op_sel_hi:[1,0]
	v_pk_mul_f32 v[48:49], v[48:49], v[152:153] op_sel_hi:[1,0]
	v_cvt_pk_bf16_f32 v54, v54, v55
	v_cvt_pk_bf16_f32 v55, v56, v57
	v_cvt_pk_bf16_f32 v56, v46, v47
	v_cvt_pk_bf16_f32 v57, v48, v49
	global_store_dwordx4 v[174:175], v[54:57], off offset:256
	s_mov_b64 s[40:41], 0xea000
	v_lshl_add_u64 v[176:177], v[172:173], 0, s[40:41]
	v_pk_mul_f32 v[50:51], v[50:51], v[154:155] op_sel_hi:[1,0]
	v_pk_mul_f32 v[52:53], v[52:53], v[154:155] op_sel_hi:[1,0]
	v_pk_mul_f32 v[42:43], v[42:43], v[154:155] op_sel_hi:[1,0]
	v_pk_mul_f32 v[44:45], v[44:45], v[154:155] op_sel_hi:[1,0]
	v_cvt_pk_bf16_f32 v50, v50, v51
	v_cvt_pk_bf16_f32 v51, v52, v53
	v_cvt_pk_bf16_f32 v52, v42, v43
	v_cvt_pk_bf16_f32 v53, v44, v45
	global_store_dwordx4 v[176:177], v[50:53], off
	v_pk_mul_f32 v[38:39], v[38:39], v[154:155] op_sel_hi:[1,0]
	v_pk_mul_f32 v[40:41], v[40:41], v[154:155] op_sel_hi:[1,0]
	v_pk_mul_f32 v[30:31], v[30:31], v[154:155] op_sel_hi:[1,0]
	v_pk_mul_f32 v[32:33], v[32:33], v[154:155] op_sel_hi:[1,0]
	v_cvt_pk_bf16_f32 v38, v38, v39
	v_cvt_pk_bf16_f32 v39, v40, v41
	v_cvt_pk_bf16_f32 v40, v30, v31
	v_cvt_pk_bf16_f32 v41, v32, v33
	global_store_dwordx4 v[176:177], v[38:41], off offset:256
	s_mov_b64 s[40:41], 0x104000
	v_lshl_add_u64 v[174:175], v[172:173], 0, s[40:41]
	v_pk_mul_f32 v[34:35], v[34:35], v[156:157] op_sel_hi:[1,0]
	v_pk_mul_f32 v[36:37], v[36:37], v[156:157] op_sel_hi:[1,0]
	v_pk_mul_f32 v[26:27], v[26:27], v[156:157] op_sel_hi:[1,0]
	v_pk_mul_f32 v[28:29], v[28:29], v[156:157] op_sel_hi:[1,0]
	v_cvt_pk_bf16_f32 v34, v34, v35
	v_cvt_pk_bf16_f32 v35, v36, v37
	v_cvt_pk_bf16_f32 v36, v26, v27
	v_cvt_pk_bf16_f32 v37, v28, v29
	global_store_dwordx4 v[174:175], v[34:37], off
	v_pk_mul_f32 v[22:23], v[22:23], v[156:157] op_sel_hi:[1,0]
	v_pk_mul_f32 v[24:25], v[24:25], v[156:157] op_sel_hi:[1,0]
	v_pk_mul_f32 v[14:15], v[14:15], v[156:157] op_sel_hi:[1,0]
	v_pk_mul_f32 v[16:17], v[16:17], v[156:157] op_sel_hi:[1,0]
	v_cvt_pk_bf16_f32 v22, v22, v23
	v_cvt_pk_bf16_f32 v23, v24, v25
	v_cvt_pk_bf16_f32 v24, v14, v15
	v_cvt_pk_bf16_f32 v25, v16, v17
	global_store_dwordx4 v[174:175], v[22:25], off offset:256
	s_mov_b64 s[40:41], 0x11e000
	v_lshl_add_u64 v[176:177], v[172:173], 0, s[40:41]
	v_pk_mul_f32 v[18:19], v[18:19], v[168:169] op_sel_hi:[1,0]
	v_pk_mul_f32 v[20:21], v[20:21], v[168:169] op_sel_hi:[1,0]
	v_pk_mul_f32 v[10:11], v[10:11], v[168:169] op_sel_hi:[1,0]
	v_pk_mul_f32 v[12:13], v[12:13], v[168:169] op_sel_hi:[1,0]
	v_cvt_pk_bf16_f32 v18, v18, v19
	v_cvt_pk_bf16_f32 v19, v20, v21
	v_cvt_pk_bf16_f32 v20, v10, v11
	v_cvt_pk_bf16_f32 v21, v12, v13
	global_store_dwordx4 v[176:177], v[18:21], off
	v_pk_mul_f32 v[6:7], v[6:7], v[168:169] op_sel_hi:[1,0]
	v_pk_mul_f32 v[8:9], v[8:9], v[168:169] op_sel_hi:[1,0]
	v_pk_mul_f32 v[2:3], v[2:3], v[168:169] op_sel_hi:[1,0]
	v_pk_mul_f32 v[4:5], v[4:5], v[168:169] op_sel_hi:[1,0]
	v_cvt_pk_bf16_f32 v6, v6, v7
	v_cvt_pk_bf16_f32 v7, v8, v9
	v_cvt_pk_bf16_f32 v8, v2, v3
	v_cvt_pk_bf16_f32 v9, v4, v5
	global_store_dwordx4 v[176:177], v[6:9], off offset:256
	s_nop 3
	v_mfma_f32_32x32x16_bf16 v[2:17], v[200:203], v[200:203], 0
	v_mfma_f32_32x32x16_bf16 v[18:33], v[200:203], v[200:203], 0
	v_mfma_f32_32x32x16_bf16 v[34:49], v[200:203], v[200:203], 0
	v_mfma_f32_32x32x16_bf16 v[50:65], v[200:203], v[200:203], 0
	v_mfma_f32_32x32x16_bf16 v[66:81], v[200:203], v[200:203], 0
	v_mfma_f32_32x32x16_bf16 v[82:97], v[200:203], v[200:203], 0
	v_mfma_f32_32x32x16_bf16 v[98:113], v[200:203], v[200:203], 0
	v_mfma_f32_32x32x16_bf16 v[114:129], v[200:203], v[200:203], 0
	s_andn2_b64 vcc, exec, s[38:39]
	s_mov_b64 s[6:7], -1
	s_cbranch_vccnz .LBB0_832
	s_andn2_b64 vcc, exec, s[12:13]
	s_cbranch_vccnz .LBB0_831
	s_branch .LBB0_831

.Lskipz_c6:
	v_and_b32_e32 v130, 8, v182
	v_and_b32_e32 v131, 16, v182
	v_lshlrev_b32_e32 v130, 2, v130
	v_lshl_add_u32 v130, v131, 3, v130
	v_lshl_add_u32 v131, s4, 8, v180
	v_add_u32_e32 v130, v130, v131
	v_mov_b32_e32 v131, 0
	v_lshl_add_u64 v[130:131], v[130:131], 4, s[14:15]
	global_load_dwordx4 v[240:243], v[130:131], off
	global_load_dwordx2 v[244:245], v[130:131], off offset:256
	global_load_dword v239, v[130:131], off offset:264
	s_cmp_eq_u32 s46, 1
	s_cbranch_scc1 .Lnobar_c6
	s_and_b64 vcc, exec, s[10:11]
	s_cbranch_vccz .Lnobar_c6
	s_barrier
.Lnobar_c6:
.LBB0_2626:
	s_add_u32 s26, s6, 0xfffc0080
	s_addc_u32 s27, s7, -1
	s_add_i32 s50, 0, 0x10000
	s_cmp_eq_u32 s49, 12
	s_cselect_b32 s29, s21, s27
	s_cselect_b32 s28, s33, s26
	v_add_u32_e32 v0, s50, v181
	s_cselect_b32 s27, s19, s48
	s_cselect_b32 s26, s40, s41
	s_add_i32 s58, 0, 0x14000
	ds_read_b128 v[130:133], v0
	ds_read_b128 v[134:137], v0 offset:1024
	ds_read_b128 v[138:141], v0 offset:2048
	ds_read_b128 v[142:145], v0 offset:3072
	v_add_u32_e32 v0, s58, v181
	ds_read_b128 v[146:149], v0
	ds_read_b128 v[150:153], v0 offset:1024
	ds_read_b128 v[154:157], v0 offset:2048
	ds_read_b128 v[170:173], v0 offset:3072
	v_lshl_add_u64 v[178:179], s[6:7], 0, v[168:169]
	s_add_i32 m0, s36, 0xc000
	ds_read_b128 v[174:177], v183
	ds_read_b128 v[184:187], v183 offset:1024
	ds_read_b128 v[188:191], v183 offset:2048
	ds_read_b128 v[192:195], v183 offset:3072
	ds_read_b128 v[196:199], v183 offset:4096
	ds_read_b128 v[200:203], v183 offset:5120
	ds_read_b128 v[204:207], v183 offset:6144
	ds_read_b128 v[216:219], v183 offset:7168
	global_load_lds_dwordx4 v[178:179], off
	v_lshl_add_u64 v[178:179], s[6:7], 0, v[166:167]
	s_add_i32 m0, s36, 0xe000
	s_nop 0
	global_load_lds_dwordx4 v[178:179], off
	s_waitcnt vmcnt(8)
	s_waitcnt lgkmcnt(0)
	s_barrier
	s_setprio 1
	s_waitcnt lgkmcnt(0)
	v_mfma_f32_16x16x32_bf16 v[126:129], v[130:133], v[174:177], v[126:129]
	v_mfma_f32_16x16x32_bf16 v[122:125], v[138:141], v[174:177], v[122:125]
	v_mfma_f32_16x16x32_bf16 v[110:113], v[130:133], v[188:191], v[110:113]
	v_mfma_f32_16x16x32_bf16 v[106:109], v[138:141], v[188:191], v[106:109]
	v_mfma_f32_16x16x32_bf16 v[94:97], v[130:133], v[196:199], v[94:97]
	v_mfma_f32_16x16x32_bf16 v[90:93], v[138:141], v[196:199], v[90:93]
	v_mfma_f32_16x16x32_bf16 v[78:81], v[130:133], v[204:207], v[78:81]
	v_mfma_f32_16x16x32_bf16 v[74:77], v[138:141], v[204:207], v[74:77]
	v_mfma_f32_16x16x32_bf16 v[126:129], v[134:137], v[184:187], v[126:129]
	v_mfma_f32_16x16x32_bf16 v[122:125], v[142:145], v[184:187], v[122:125]
	v_mfma_f32_16x16x32_bf16 v[110:113], v[134:137], v[192:195], v[110:113]
	v_mfma_f32_16x16x32_bf16 v[106:109], v[142:145], v[192:195], v[106:109]
	v_mfma_f32_16x16x32_bf16 v[94:97], v[134:137], v[200:203], v[94:97]
	v_mfma_f32_16x16x32_bf16 v[90:93], v[142:145], v[200:203], v[90:93]
	v_mfma_f32_16x16x32_bf16 v[78:81], v[134:137], v[216:219], v[78:81]
	v_mfma_f32_16x16x32_bf16 v[74:77], v[142:145], v[216:219], v[74:77]
	s_setprio 0
	s_setprio 1
	v_mfma_f32_16x16x32_bf16 v[118:121], v[146:149], v[174:177], v[118:121]
	v_mfma_f32_16x16x32_bf16 v[114:117], v[154:157], v[174:177], v[114:117]
	v_mfma_f32_16x16x32_bf16 v[102:105], v[146:149], v[188:191], v[102:105]
	v_mfma_f32_16x16x32_bf16 v[98:101], v[154:157], v[188:191], v[98:101]
	v_mfma_f32_16x16x32_bf16 v[86:89], v[146:149], v[196:199], v[86:89]
	v_mfma_f32_16x16x32_bf16 v[82:85], v[154:157], v[196:199], v[82:85]
	v_mfma_f32_16x16x32_bf16 v[70:73], v[146:149], v[204:207], v[70:73]
	v_mfma_f32_16x16x32_bf16 v[66:69], v[154:157], v[204:207], v[66:69]
	v_mfma_f32_16x16x32_bf16 v[118:121], v[150:153], v[184:187], v[118:121]
	v_mfma_f32_16x16x32_bf16 v[114:117], v[170:173], v[184:187], v[114:117]
	v_mfma_f32_16x16x32_bf16 v[102:105], v[150:153], v[192:195], v[102:105]
	v_mfma_f32_16x16x32_bf16 v[98:101], v[170:173], v[192:195], v[98:101]
	v_mfma_f32_16x16x32_bf16 v[86:89], v[150:153], v[200:203], v[86:89]
	v_mfma_f32_16x16x32_bf16 v[82:85], v[170:173], v[200:203], v[82:85]
	v_mfma_f32_16x16x32_bf16 v[70:73], v[150:153], v[216:219], v[70:73]
	v_mfma_f32_16x16x32_bf16 v[66:69], v[170:173], v[216:219], v[66:69]
	s_setprio 0
	s_barrier
	s_add_i32 s50, s50, s35
	v_lshl_add_u64 v[178:179], s[26:27], 0, v[162:163]
	s_mov_b32 m0, s50
	ds_read_b128 v[174:177], v183 offset:16384
	ds_read_b128 v[184:187], v183 offset:17408
	ds_read_b128 v[188:191], v183 offset:18432
	ds_read_b128 v[192:195], v183 offset:19456
	ds_read_b128 v[196:199], v183 offset:20480
	ds_read_b128 v[200:203], v183 offset:21504
	ds_read_b128 v[204:207], v183 offset:22528
	ds_read_b128 v[216:219], v183 offset:23552
	global_load_lds_dwordx4 v[178:179], off
	s_add_i32 m0, s50, 0x2000
	s_add_u32 s52, s26, 0x40000
	v_lshl_add_u64 v[208:209], s[26:27], 0, v[158:159]
	s_addc_u32 s53, s27, 0
	s_add_i32 s50, s58, s35
	global_load_lds_dwordx4 v[208:209], off
	v_lshl_add_u64 v[220:221], s[52:53], 0, v[162:163]
	s_mov_b32 m0, s50
	v_lshl_add_u64 v[222:223], s[28:29], 0, v[160:161]
	global_load_lds_dwordx4 v[220:221], off
	v_lshl_add_u64 v[220:221], s[52:53], 0, v[158:159]
	s_add_i32 m0, s50, 0x2000
	s_nop 0
	global_load_lds_dwordx4 v[220:221], off
	v_lshl_add_u64 v[220:221], s[28:29], 0, v[164:165]
	s_mov_b32 m0, s36
	s_nop 0
	global_load_lds_dwordx4 v[220:221], off
	s_mov_b32 m0, s37
	s_nop 0
	global_load_lds_dwordx4 v[222:223], off
	s_waitcnt vmcnt(8)
	s_waitcnt lgkmcnt(0)
	s_barrier
	s_setprio 1
	s_waitcnt lgkmcnt(0)
	v_mfma_f32_16x16x32_bf16 v[62:65], v[130:133], v[174:177], v[62:65]
	v_mfma_f32_16x16x32_bf16 v[58:61], v[138:141], v[174:177], v[58:61]
	v_mfma_f32_16x16x32_bf16 v[46:49], v[130:133], v[188:191], v[46:49]
	v_mfma_f32_16x16x32_bf16 v[42:45], v[138:141], v[188:191], v[42:45]
	v_mfma_f32_16x16x32_bf16 v[30:33], v[130:133], v[196:199], v[30:33]
	v_mfma_f32_16x16x32_bf16 v[26:29], v[138:141], v[196:199], v[26:29]
	v_mfma_f32_16x16x32_bf16 v[14:17], v[130:133], v[204:207], v[14:17]
	v_mfma_f32_16x16x32_bf16 v[10:13], v[138:141], v[204:207], v[10:13]
	v_mfma_f32_16x16x32_bf16 v[62:65], v[134:137], v[184:187], v[62:65]
	v_mfma_f32_16x16x32_bf16 v[58:61], v[142:145], v[184:187], v[58:61]
	v_mfma_f32_16x16x32_bf16 v[46:49], v[134:137], v[192:195], v[46:49]
	v_mfma_f32_16x16x32_bf16 v[42:45], v[142:145], v[192:195], v[42:45]
	v_mfma_f32_16x16x32_bf16 v[30:33], v[134:137], v[200:203], v[30:33]
	v_mfma_f32_16x16x32_bf16 v[26:29], v[142:145], v[200:203], v[26:29]
	v_mfma_f32_16x16x32_bf16 v[14:17], v[134:137], v[216:219], v[14:17]
	v_mfma_f32_16x16x32_bf16 v[10:13], v[142:145], v[216:219], v[10:13]
	s_setprio 0
	s_setprio 1
	v_mfma_f32_16x16x32_bf16 v[54:57], v[146:149], v[174:177], v[54:57]
	v_mfma_f32_16x16x32_bf16 v[50:53], v[154:157], v[174:177], v[50:53]
	v_mfma_f32_16x16x32_bf16 v[38:41], v[146:149], v[188:191], v[38:41]
	v_mfma_f32_16x16x32_bf16 v[34:37], v[154:157], v[188:191], v[34:37]
	v_mfma_f32_16x16x32_bf16 v[22:25], v[146:149], v[196:199], v[22:25]
	v_mfma_f32_16x16x32_bf16 v[18:21], v[154:157], v[196:199], v[18:21]
	v_mfma_f32_16x16x32_bf16 v[6:9], v[146:149], v[204:207], v[6:9]
	v_mfma_f32_16x16x32_bf16 v[2:5], v[154:157], v[204:207], v[2:5]
	v_mfma_f32_16x16x32_bf16 v[54:57], v[150:153], v[184:187], v[54:57]
	v_mfma_f32_16x16x32_bf16 v[50:53], v[170:173], v[184:187], v[50:53]
	v_mfma_f32_16x16x32_bf16 v[38:41], v[150:153], v[192:195], v[38:41]
	v_mfma_f32_16x16x32_bf16 v[34:37], v[170:173], v[192:195], v[34:37]
	v_mfma_f32_16x16x32_bf16 v[22:25], v[150:153], v[200:203], v[22:25]
	v_mfma_f32_16x16x32_bf16 v[18:21], v[170:173], v[200:203], v[18:21]
	v_mfma_f32_16x16x32_bf16 v[6:9], v[150:153], v[216:219], v[6:9]
	v_mfma_f32_16x16x32_bf16 v[2:5], v[170:173], v[216:219], v[2:5]
	s_setprio 0
	s_barrier
	s_add_i32 s50, 0, 0x18000
	v_add_u32_e32 v0, s50, v181
	s_add_i32 s52, 0, 0x1c000
	ds_read_b128 v[130:133], v0
	ds_read_b128 v[134:137], v0 offset:1024
	ds_read_b128 v[138:141], v0 offset:2048
	ds_read_b128 v[142:145], v0 offset:3072
	v_add_u32_e32 v0, s52, v181
	ds_read_b128 v[146:149], v0
	ds_read_b128 v[150:153], v0 offset:1024
	ds_read_b128 v[154:157], v0 offset:2048
	ds_read_b128 v[170:173], v0 offset:3072
	s_add_u32 s28, s28, 0x40000
	s_addc_u32 s29, s29, 0
	s_mov_b32 m0, s42
	v_lshl_add_u64 v[224:225], s[28:29], 0, v[164:165]
	ds_read_b128 v[174:177], v183 offset:32768
	ds_read_b128 v[184:187], v183 offset:33792
	ds_read_b128 v[188:191], v183 offset:34816
	ds_read_b128 v[192:195], v183 offset:35840
	ds_read_b128 v[196:199], v183 offset:36864
	ds_read_b128 v[200:203], v183 offset:37888
	ds_read_b128 v[204:207], v183 offset:38912
	ds_read_b128 v[216:219], v183 offset:39936
	global_load_lds_dwordx4 v[224:225], off
	v_lshl_add_u64 v[224:225], s[28:29], 0, v[160:161]
	s_mov_b32 m0, s43
	s_nop 0
	global_load_lds_dwordx4 v[224:225], off
	s_waitcnt vmcnt(8)
	s_waitcnt lgkmcnt(0)
	s_barrier
	s_setprio 1
	s_waitcnt lgkmcnt(0)
	v_mfma_f32_16x16x32_bf16 v[126:129], v[130:133], v[174:177], v[126:129]
	v_mfma_f32_16x16x32_bf16 v[122:125], v[138:141], v[174:177], v[122:125]
	v_mfma_f32_16x16x32_bf16 v[110:113], v[130:133], v[188:191], v[110:113]
	v_mfma_f32_16x16x32_bf16 v[106:109], v[138:141], v[188:191], v[106:109]
	v_mfma_f32_16x16x32_bf16 v[94:97], v[130:133], v[196:199], v[94:97]
	v_mfma_f32_16x16x32_bf16 v[90:93], v[138:141], v[196:199], v[90:93]
	v_mfma_f32_16x16x32_bf16 v[78:81], v[130:133], v[204:207], v[78:81]
	v_mfma_f32_16x16x32_bf16 v[74:77], v[138:141], v[204:207], v[74:77]
	v_mfma_f32_16x16x32_bf16 v[126:129], v[134:137], v[184:187], v[126:129]
	v_mfma_f32_16x16x32_bf16 v[122:125], v[142:145], v[184:187], v[122:125]
	v_mfma_f32_16x16x32_bf16 v[110:113], v[134:137], v[192:195], v[110:113]
	v_mfma_f32_16x16x32_bf16 v[106:109], v[142:145], v[192:195], v[106:109]
	v_mfma_f32_16x16x32_bf16 v[94:97], v[134:137], v[200:203], v[94:97]
	v_mfma_f32_16x16x32_bf16 v[90:93], v[142:145], v[200:203], v[90:93]
	v_mfma_f32_16x16x32_bf16 v[78:81], v[134:137], v[216:219], v[78:81]
	v_mfma_f32_16x16x32_bf16 v[74:77], v[142:145], v[216:219], v[74:77]
	s_setprio 0
	s_setprio 1
	v_mfma_f32_16x16x32_bf16 v[118:121], v[146:149], v[174:177], v[118:121]
	v_mfma_f32_16x16x32_bf16 v[114:117], v[154:157], v[174:177], v[114:117]
	v_mfma_f32_16x16x32_bf16 v[102:105], v[146:149], v[188:191], v[102:105]
	v_mfma_f32_16x16x32_bf16 v[98:101], v[154:157], v[188:191], v[98:101]
	v_mfma_f32_16x16x32_bf16 v[86:89], v[146:149], v[196:199], v[86:89]
	v_mfma_f32_16x16x32_bf16 v[82:85], v[154:157], v[196:199], v[82:85]
	v_mfma_f32_16x16x32_bf16 v[70:73], v[146:149], v[204:207], v[70:73]
	v_mfma_f32_16x16x32_bf16 v[66:69], v[154:157], v[204:207], v[66:69]
	v_mfma_f32_16x16x32_bf16 v[118:121], v[150:153], v[184:187], v[118:121]
	v_mfma_f32_16x16x32_bf16 v[114:117], v[170:173], v[184:187], v[114:117]
	v_mfma_f32_16x16x32_bf16 v[102:105], v[150:153], v[192:195], v[102:105]
	v_mfma_f32_16x16x32_bf16 v[98:101], v[170:173], v[192:195], v[98:101]
	v_mfma_f32_16x16x32_bf16 v[86:89], v[150:153], v[200:203], v[86:89]
	v_mfma_f32_16x16x32_bf16 v[82:85], v[170:173], v[200:203], v[82:85]
	v_mfma_f32_16x16x32_bf16 v[70:73], v[150:153], v[216:219], v[70:73]
	v_mfma_f32_16x16x32_bf16 v[66:69], v[170:173], v[216:219], v[66:69]
	s_setprio 0
	s_barrier
	s_add_i32 s28, s50, s35
	v_lshl_add_u64 v[178:179], v[178:179], 0, s[56:57]
	s_mov_b32 m0, s28
	ds_read_b128 v[174:177], v183 offset:49152
	ds_read_b128 v[184:187], v183 offset:50176
	ds_read_b128 v[188:191], v183 offset:51200
	ds_read_b128 v[192:195], v183 offset:52224
	ds_read_b128 v[196:199], v183 offset:53248
	ds_read_b128 v[200:203], v183 offset:54272
	ds_read_b128 v[204:207], v183 offset:55296
	ds_read_b128 v[216:219], v183 offset:56320
	global_load_lds_dwordx4 v[178:179], off
	s_add_i32 m0, s28, 0x2000
	s_add_u32 s26, s26, 0x40080
	v_lshl_add_u64 v[178:179], v[208:209], 0, s[56:57]
	s_addc_u32 s27, s27, 0
	s_add_i32 s28, s52, s35
	global_load_lds_dwordx4 v[178:179], off
	v_lshl_add_u64 v[178:179], s[26:27], 0, v[162:163]
	s_mov_b32 m0, s28
	s_nop 0
	global_load_lds_dwordx4 v[178:179], off
	v_lshl_add_u64 v[178:179], s[26:27], 0, v[158:159]
	s_add_i32 m0, s28, 0x2000
	s_nop 0
	global_load_lds_dwordx4 v[178:179], off
	v_lshl_add_u64 v[178:179], v[220:221], 0, s[56:57]
	s_mov_b32 m0, s44
	s_nop 0
	global_load_lds_dwordx4 v[178:179], off
	v_lshl_add_u64 v[178:179], v[222:223], 0, s[56:57]
	s_mov_b32 m0, s45
	s_nop 0
	global_load_lds_dwordx4 v[178:179], off
	s_waitcnt vmcnt(8)
	s_waitcnt lgkmcnt(0)
	s_barrier
	s_setprio 1
	s_waitcnt lgkmcnt(0)
	v_mfma_f32_16x16x32_bf16 v[62:65], v[130:133], v[174:177], v[62:65]
	v_mfma_f32_16x16x32_bf16 v[58:61], v[138:141], v[174:177], v[58:61]
	v_mfma_f32_16x16x32_bf16 v[46:49], v[130:133], v[188:191], v[46:49]
	v_mfma_f32_16x16x32_bf16 v[42:45], v[138:141], v[188:191], v[42:45]
	v_mfma_f32_16x16x32_bf16 v[30:33], v[130:133], v[196:199], v[30:33]
	v_mfma_f32_16x16x32_bf16 v[26:29], v[138:141], v[196:199], v[26:29]
	v_mfma_f32_16x16x32_bf16 v[14:17], v[130:133], v[204:207], v[14:17]
	v_mfma_f32_16x16x32_bf16 v[10:13], v[138:141], v[204:207], v[10:13]
	v_mfma_f32_16x16x32_bf16 v[62:65], v[134:137], v[184:187], v[62:65]
	v_mfma_f32_16x16x32_bf16 v[58:61], v[142:145], v[184:187], v[58:61]
	v_mfma_f32_16x16x32_bf16 v[46:49], v[134:137], v[192:195], v[46:49]
	v_mfma_f32_16x16x32_bf16 v[42:45], v[142:145], v[192:195], v[42:45]
	v_mfma_f32_16x16x32_bf16 v[30:33], v[134:137], v[200:203], v[30:33]
	v_mfma_f32_16x16x32_bf16 v[26:29], v[142:145], v[200:203], v[26:29]
	v_mfma_f32_16x16x32_bf16 v[14:17], v[134:137], v[216:219], v[14:17]
	v_mfma_f32_16x16x32_bf16 v[10:13], v[142:145], v[216:219], v[10:13]
	s_setprio 0
	s_setprio 1
	v_mfma_f32_16x16x32_bf16 v[54:57], v[146:149], v[174:177], v[54:57]
	v_mfma_f32_16x16x32_bf16 v[50:53], v[154:157], v[174:177], v[50:53]
	v_mfma_f32_16x16x32_bf16 v[38:41], v[146:149], v[188:191], v[38:41]
	v_mfma_f32_16x16x32_bf16 v[34:37], v[154:157], v[188:191], v[34:37]
	v_mfma_f32_16x16x32_bf16 v[22:25], v[146:149], v[196:199], v[22:25]
	v_mfma_f32_16x16x32_bf16 v[18:21], v[154:157], v[196:199], v[18:21]
	v_mfma_f32_16x16x32_bf16 v[6:9], v[146:149], v[204:207], v[6:9]
	v_mfma_f32_16x16x32_bf16 v[2:5], v[154:157], v[204:207], v[2:5]
	v_mfma_f32_16x16x32_bf16 v[54:57], v[150:153], v[184:187], v[54:57]
	v_mfma_f32_16x16x32_bf16 v[50:53], v[170:173], v[184:187], v[50:53]
	v_mfma_f32_16x16x32_bf16 v[38:41], v[150:153], v[192:195], v[38:41]
	v_mfma_f32_16x16x32_bf16 v[34:37], v[170:173], v[192:195], v[34:37]
	v_mfma_f32_16x16x32_bf16 v[22:25], v[150:153], v[200:203], v[22:25]
	v_mfma_f32_16x16x32_bf16 v[18:21], v[170:173], v[200:203], v[18:21]
	v_mfma_f32_16x16x32_bf16 v[6:9], v[150:153], v[216:219], v[6:9]
	v_mfma_f32_16x16x32_bf16 v[2:5], v[170:173], v[216:219], v[2:5]
	s_setprio 0
	s_barrier
	s_add_i32 s49, s49, 2
	s_add_u32 s41, s41, 0x100
	s_addc_u32 s48, s48, 0
	s_add_u32 s6, s6, 0x100
	s_addc_u32 s7, s7, 0
	s_cmp_gt_u32 s49, 13
	s_cbranch_scc0 .LBB0_2626
	s_and_b64 vcc, exec, s[16:17]
	s_cbranch_vccz .LBB0_2629
	s_barrier
